# strategy 8: ml_out P.V chain, two of three V^T fragment reads per output group issued unconditionally at group start into spare quads (MFMA shadow)
# speedup vs baseline: 1.0050x; 1.0013x over previous
.LBB0_910:
	s_or_b64 exec, exec, s[50:51]
	s_waitcnt lgkmcnt(0)
	v_add_u32_e32 v1, s52, v215
	s_waitcnt lgkmcnt(0)
	ds_read_b128 v[138:141], v1 offset:37904
	ds_read_b128 v[142:145], v1 offset:37968
	ds_read2_b64 v[242:245], v216 offset0:8 offset1:12
	ds_read2_b64 v[246:249], v216 offset0:16 offset1:20
	s_or_b64 s[52:53], s[58:59], s[76:77]
	v_cndmask_b32_e64 v1, 0, 1, s[52:53]
	v_cmp_ne_u32_e64 s[50:51], 1, v1
	s_andn2_b64 vcc, exec, s[52:53]
	s_cbranch_vccnz .LBB0_912
	ds_read2_b64 v[146:149], v216 offset1:4
	s_waitcnt lgkmcnt(0)
	v_mfma_f32_16x16x32_bf16 v[146:149], v[90:93], v[146:149], 0
	s_branch .LBB0_913

.LBB0_913:
	v_cndmask_b32_e64 v1, 0, 1, s[64:65]
	v_cndmask_b32_e64 v165, 0, 1, s[66:67]
	s_and_b64 s[52:53], s[76:77], exec
	v_readfirstlane_b32 s52, v165
	v_readfirstlane_b32 s53, v1
	s_cselect_b32 s52, s52, s53
	s_bitcmp1_b32 s52, 0
	s_cselect_b64 s[54:55], -1, 0
	s_bitcmp0_b32 s52, 0
	s_cbranch_scc1 .LBB0_915
	s_waitcnt lgkmcnt(0)
	v_mfma_f32_16x16x32_bf16 v[146:149], v[118:121], v[242:245], v[146:149]
.LBB0_915:
	v_cndmask_b32_e64 v1, 0, 1, s[68:69]
	v_cndmask_b32_e64 v165, 0, 1, s[70:71]
	s_and_b64 s[52:53], s[76:77], exec
	v_readfirstlane_b32 s52, v165
	v_readfirstlane_b32 s53, v1
	s_cselect_b32 s52, s52, s53
	s_bitcmp1_b32 s52, 0
	s_cselect_b64 s[56:57], -1, 0
	s_bitcmp0_b32 s52, 0
	s_cbranch_scc1 .LBB0_917
	s_waitcnt lgkmcnt(0)
	v_mfma_f32_16x16x32_bf16 v[146:149], v[130:133], v[246:249], v[146:149]

.LBB0_919:
	v_mfma_f32_16x16x32_bf16 v[238:241], v[2:5], v[126:129], 0
	s_mov_b32 s62, s60
	s_mov_b32 s63, s60
	s_mov_b32 s61, s60
	v_mfma_f32_16x16x32_bf16 v[122:125], v[6:9], v[122:125], v[238:241]
	v_mov_b64_e32 v[128:129], s[62:63]
	v_mov_b64_e32 v[126:127], s[60:61]
	s_and_b64 vcc, exec, s[50:51]
	v_add_u32_e32 v165, 0x1000, v216
	ds_read2_b64 v[242:245], v165 offset0:48 offset1:52
	ds_read2_b64 v[246:249], v165 offset0:40 offset1:44
	s_cbranch_vccnz .LBB0_923
	ds_read2_b64 v[126:129], v165 offset0:32 offset1:36
	s_waitcnt lgkmcnt(0)
	v_mfma_f32_16x16x32_bf16 v[126:129], v[90:93], v[126:129], 0
	v_cndmask_b32_e64 v1, 0, 1, s[54:55]
	v_cmp_ne_u32_e64 s[52:53], 1, v1
	s_andn2_b64 vcc, exec, s[54:55]
	s_cbranch_vccz .LBB0_924

.LBB0_922:
	s_waitcnt lgkmcnt(0)
	v_mfma_f32_16x16x32_bf16 v[126:129], v[130:133], v[242:245], v[126:129]
	v_cndmask_b32_e64 v1, 0, 1, s[78:79]
	v_cmp_ne_u32_e64 s[56:57], 1, v1
	s_andn2_b64 vcc, exec, s[78:79]
	s_cbranch_vccz .LBB0_926
	s_branch .LBB0_927

.LBB0_924:
	s_waitcnt lgkmcnt(0)
	v_mfma_f32_16x16x32_bf16 v[126:129], v[118:121], v[246:249], v[126:129]
	v_cndmask_b32_e64 v1, 0, 1, s[56:57]
	v_cmp_ne_u32_e64 s[54:55], 1, v1
	s_andn2_b64 vcc, exec, s[56:57]
	s_cbranch_vccz .LBB0_922

.LBB0_927:
	v_mfma_f32_16x16x32_bf16 v[238:241], v[2:5], v[114:117], 0
	s_mov_b32 s62, s60
	s_mov_b32 s63, s60
	s_mov_b32 s61, s60
	v_mfma_f32_16x16x32_bf16 v[110:113], v[6:9], v[110:113], v[238:241]
	v_mov_b64_e32 v[116:117], s[62:63]
	v_mov_b64_e32 v[114:115], s[60:61]
	s_and_b64 vcc, exec, s[50:51]
	v_add_u32_e32 v165, 0x2000, v216
	ds_read2_b64 v[242:245], v165 offset0:80 offset1:84
	ds_read2_b64 v[246:249], v165 offset0:72 offset1:76
	s_cbranch_vccnz .LBB0_931
	ds_read2_b64 v[114:117], v165 offset0:64 offset1:68
	s_waitcnt lgkmcnt(0)
	v_mfma_f32_16x16x32_bf16 v[114:117], v[90:93], v[114:117], 0
	s_and_b64 vcc, exec, s[52:53]
	s_cbranch_vccz .LBB0_932

.LBB0_930:
	s_waitcnt lgkmcnt(0)
	v_mfma_f32_16x16x32_bf16 v[114:117], v[130:133], v[242:245], v[114:117]
	s_and_b64 vcc, exec, s[56:57]
	s_cbranch_vccz .LBB0_934
	s_branch .LBB0_935

.LBB0_932:
	s_waitcnt lgkmcnt(0)
	v_mfma_f32_16x16x32_bf16 v[114:117], v[118:121], v[246:249], v[114:117]
	s_and_b64 vcc, exec, s[54:55]
	s_cbranch_vccz .LBB0_930

.LBB0_935:
	v_mfma_f32_16x16x32_bf16 v[238:241], v[2:5], v[106:109], 0
	s_mov_b32 s62, s60
	s_mov_b32 s63, s60
	s_mov_b32 s61, s60
	v_mfma_f32_16x16x32_bf16 v[102:105], v[6:9], v[102:105], v[238:241]
	v_mov_b64_e32 v[108:109], s[62:63]
	v_mov_b64_e32 v[106:107], s[60:61]
	s_and_b64 vcc, exec, s[50:51]
	v_add_u32_e32 v165, 0x3000, v216
	ds_read2_b64 v[242:245], v165 offset0:112 offset1:116
	ds_read2_b64 v[246:249], v165 offset0:104 offset1:108
	s_cbranch_vccnz .LBB0_939
	ds_read2_b64 v[106:109], v165 offset0:96 offset1:100
	s_waitcnt lgkmcnt(0)
	v_mfma_f32_16x16x32_bf16 v[106:109], v[90:93], v[106:109], 0
	s_and_b64 vcc, exec, s[52:53]
	s_cbranch_vccz .LBB0_940

.LBB0_938:
	s_waitcnt lgkmcnt(0)
	v_mfma_f32_16x16x32_bf16 v[106:109], v[130:133], v[242:245], v[106:109]
	s_and_b64 vcc, exec, s[56:57]
	s_cbranch_vccz .LBB0_942
	s_branch .LBB0_943

.LBB0_940:
	s_waitcnt lgkmcnt(0)
	v_mfma_f32_16x16x32_bf16 v[106:109], v[118:121], v[246:249], v[106:109]
	s_and_b64 vcc, exec, s[54:55]
	s_cbranch_vccz .LBB0_938

.LBB0_943:
	v_mfma_f32_16x16x32_bf16 v[238:241], v[2:5], v[98:101], 0
	s_mov_b32 s62, s60
	s_mov_b32 s63, s60
	s_mov_b32 s61, s60
	v_mfma_f32_16x16x32_bf16 v[94:97], v[6:9], v[94:97], v[238:241]
	v_mov_b64_e32 v[100:101], s[62:63]
	v_mov_b64_e32 v[98:99], s[60:61]
	s_and_b64 vcc, exec, s[50:51]
	v_add_u32_e32 v165, 0x4000, v216
	ds_read2_b64 v[242:245], v165 offset0:144 offset1:148
	ds_read2_b64 v[246:249], v165 offset0:136 offset1:140
	s_cbranch_vccnz .LBB0_947
	ds_read2_b64 v[98:101], v165 offset0:128 offset1:132
	s_waitcnt lgkmcnt(0)
	v_mfma_f32_16x16x32_bf16 v[98:101], v[90:93], v[98:101], 0
	s_and_b64 vcc, exec, s[52:53]
	s_cbranch_vccz .LBB0_948

.LBB0_946:
	s_waitcnt lgkmcnt(0)
	v_mfma_f32_16x16x32_bf16 v[98:101], v[130:133], v[242:245], v[98:101]
	s_and_b64 vcc, exec, s[56:57]
	s_cbranch_vccz .LBB0_950
	s_branch .LBB0_951

.LBB0_948:
	s_waitcnt lgkmcnt(0)
	v_mfma_f32_16x16x32_bf16 v[98:101], v[118:121], v[246:249], v[98:101]
	s_and_b64 vcc, exec, s[54:55]
	s_cbranch_vccz .LBB0_946

.LBB0_951:
	v_mfma_f32_16x16x32_bf16 v[238:241], v[2:5], v[86:89], 0
	s_mov_b32 s62, s60
	s_mov_b32 s63, s60
	s_mov_b32 s61, s60
	v_mfma_f32_16x16x32_bf16 v[82:85], v[6:9], v[82:85], v[238:241]
	v_mov_b64_e32 v[88:89], s[62:63]
	v_mov_b64_e32 v[86:87], s[60:61]
	s_and_b64 vcc, exec, s[50:51]
	v_add_u32_e32 v165, 0x5000, v216
	ds_read2_b64 v[242:245], v165 offset0:176 offset1:180
	ds_read2_b64 v[246:249], v165 offset0:168 offset1:172
	s_cbranch_vccnz .LBB0_955
	ds_read2_b64 v[86:89], v165 offset0:160 offset1:164
	s_waitcnt lgkmcnt(0)
	v_mfma_f32_16x16x32_bf16 v[86:89], v[90:93], v[86:89], 0
	s_and_b64 vcc, exec, s[52:53]
	s_cbranch_vccz .LBB0_956

.LBB0_954:
	s_waitcnt lgkmcnt(0)
	v_mfma_f32_16x16x32_bf16 v[86:89], v[130:133], v[242:245], v[86:89]
	s_and_b64 vcc, exec, s[56:57]
	s_cbranch_vccz .LBB0_958
	s_branch .LBB0_959

.LBB0_956:
	s_waitcnt lgkmcnt(0)
	v_mfma_f32_16x16x32_bf16 v[86:89], v[118:121], v[246:249], v[86:89]
	s_and_b64 vcc, exec, s[54:55]
	s_cbranch_vccz .LBB0_954

.LBB0_959:
	v_mfma_f32_16x16x32_bf16 v[238:241], v[2:5], v[78:81], 0
	s_mov_b32 s62, s60
	s_mov_b32 s63, s60
	s_mov_b32 s61, s60
	v_mfma_f32_16x16x32_bf16 v[74:77], v[6:9], v[74:77], v[238:241]
	v_mov_b64_e32 v[80:81], s[62:63]
	v_mov_b64_e32 v[78:79], s[60:61]
	s_and_b64 vcc, exec, s[50:51]
	v_add_u32_e32 v165, 0x6000, v216
	ds_read2_b64 v[242:245], v165 offset0:208 offset1:212
	ds_read2_b64 v[246:249], v165 offset0:200 offset1:204
	s_cbranch_vccnz .LBB0_963
	ds_read2_b64 v[78:81], v165 offset0:192 offset1:196
	s_waitcnt lgkmcnt(0)
	v_mfma_f32_16x16x32_bf16 v[78:81], v[90:93], v[78:81], 0
	s_and_b64 vcc, exec, s[52:53]
	s_cbranch_vccz .LBB0_964

.LBB0_962:
	s_waitcnt lgkmcnt(0)
	v_mfma_f32_16x16x32_bf16 v[78:81], v[130:133], v[242:245], v[78:81]
	s_and_b64 vcc, exec, s[56:57]
	s_cbranch_vccz .LBB0_966
	s_branch .LBB0_967

.LBB0_964:
	s_waitcnt lgkmcnt(0)
	v_mfma_f32_16x16x32_bf16 v[78:81], v[118:121], v[246:249], v[78:81]
	s_and_b64 vcc, exec, s[54:55]
	s_cbranch_vccz .LBB0_962
